# stick-breaking attention: next task id fetched (atomic) at the start of the current task, no vmcnt(0) between tasks; on top of the K/V load de-serialisation
# baseline (speedup 1.0000x reference)
.LBB0_445:
	s_and_b32 s4, s41, 7
	s_lshl_b32 s43, s4, 12
	s_add_i32 s4, s37, s36
	s_and_b32 s10, s4, 7
	s_lshl_b32 s4, s10, 8
	s_add_u32 s4, s34, s4
	s_addc_u32 s5, s35, 0
	s_waitcnt lgkmcnt(0)
	s_lshl_b32 s46, s10, 12
	s_and_saveexec_b64 s[12:13], s[8:9]
	v_mov_b32_e32 v219, 1
	global_atomic_add v219, v161, v219, s[4:5] sc0
	s_mov_b64 exec, s[12:13]
	s_waitcnt vmcnt(0)
	s_branch .LBB0_448

.LBB0_448:
	v_readfirstlane_b32 s10, v219
	s_cmpk_gt_i32 s10, 0x7ff
	s_cselect_b64 s[30:31], -1, 0
	s_and_b64 vcc, exec, s[30:31]
	s_cbranch_vccnz .LBB0_447
	s_and_saveexec_b64 s[12:13], s[8:9]
	v_mov_b32_e32 v219, 1
	global_atomic_add v219, v161, v219, s[4:5] sc0
	s_mov_b64 exec, s[12:13]
	s_lshl_b32 s14, s10, 1
	s_and_b32 s47, s10, 0x780
	s_lshl_b32 s11, s10, 5
	s_add_i32 s10, s14, s46
	s_and_b32 s56, s11, 0xfe0
	s_and_b32 s57, s10, 0xfffff000
	s_or_b32 s15, s57, s56
	s_lshl_b32 s10, s47, 1
	s_add_u32 s10, s50, s10
	s_addc_u32 s11, s51, 0
	v_add_u32_e32 v32, s15, v174
	v_mov_b64_e32 v[24:25], s[10:11]
	v_add_u32_e32 v34, s15, v175
	v_add_u32_e32 v36, s15, v176
	v_add_u32_e32 v38, s15, v177
	v_add_u32_e32 v40, s15, v178
	v_add_u32_e32 v41, s15, v179
	v_mad_i64_i32 v[0:1], s[12:13], v32, s3, v[24:25]
	v_mad_i64_i32 v[2:3], s[12:13], v34, s3, v[24:25]
	v_mad_i64_i32 v[8:9], s[12:13], v36, s3, v[24:25]
	v_mad_i64_i32 v[10:11], s[12:13], v38, s3, v[24:25]
	v_mad_i64_i32 v[16:17], s[12:13], v40, s3, v[24:25]
	v_mad_i64_i32 v[18:19], s[12:13], v41, s3, v[24:25]
	v_lshl_add_u64 v[0:1], v[0:1], 0, v[160:161]
	v_lshl_add_u64 v[4:5], v[2:3], 0, v[160:161]
	v_lshl_add_u64 v[8:9], v[8:9], 0, v[160:161]
	v_lshl_add_u64 v[12:13], v[10:11], 0, v[160:161]
	v_lshl_add_u64 v[16:17], v[16:17], 0, v[160:161]
	v_lshl_add_u64 v[20:21], v[18:19], 0, v[160:161]
	global_load_dwordx4 v[0:3], v[0:1], off
	s_nop 0
	global_load_dwordx4 v[4:7], v[4:5], off
	s_nop 0
	global_load_dwordx4 v[8:11], v[8:9], off
	s_nop 0
	global_load_dwordx4 v[12:15], v[12:13], off
	s_nop 0
	global_load_dwordx4 v[16:19], v[16:17], off
	s_nop 0
	global_load_dwordx4 v[20:23], v[20:21], off
	v_mov_b32_e32 v147, v161
	v_lshl_add_u64 v[148:149], s[10:11], 0, v[146:147]
	s_mov_b64 s[98:99], 0x2000
	v_lshl_add_u64 v[216:217], v[148:149], 0, s[98:99]
	v_mad_i64_i32 v[32:33], s[10:11], v32, s3, v[148:149]
	v_add_co_u32_e32 v32, vcc, s93, v32
	v_mad_i64_i32 v[34:35], s[10:11], v34, s3, v[148:149]
	s_nop 0
	v_addc_co_u32_e32 v33, vcc, 0, v33, vcc
	v_add_co_u32_e32 v34, vcc, s93, v34
	v_mad_i64_i32 v[36:37], s[10:11], v36, s3, v[148:149]
	s_nop 0
	v_addc_co_u32_e32 v35, vcc, 0, v35, vcc
	v_add_u32_e32 v42, s15, v180
	v_add_u32_e32 v43, s15, v181
	v_add_co_u32_e32 v36, vcc, s93, v36
	v_mad_i64_i32 v[26:27], s[12:13], v42, s3, v[24:25]
	v_mad_i64_i32 v[24:25], s[12:13], v43, s3, v[24:25]
	v_mad_i64_i32 v[38:39], s[10:11], v38, s3, v[148:149]
	v_addc_co_u32_e32 v37, vcc, 0, v37, vcc
	v_lshl_add_u64 v[26:27], v[26:27], 0, v[160:161]
	v_lshl_add_u64 v[28:29], v[24:25], 0, v[160:161]
	v_add_co_u32_e32 v38, vcc, s93, v38
	global_load_dwordx4 v[24:27], v[26:27], off
	s_nop 0
	global_load_dwordx4 v[28:31], v[28:29], off
	v_addc_co_u32_e32 v39, vcc, 0, v39, vcc
	global_load_dwordx4 v[80:83], v[32:33], off offset:-4096
	global_load_dwordx4 v[84:87], v[32:33], off
	global_load_dwordx4 v[88:91], v[34:35], off offset:-4096
	global_load_dwordx4 v[92:95], v[34:35], off
	global_load_dwordx4 v[96:99], v[36:37], off offset:-4096
	global_load_dwordx4 v[100:103], v[36:37], off
	global_load_dwordx4 v[104:107], v[38:39], off offset:-4096
	global_load_dwordx4 v[108:111], v[38:39], off
	v_mad_i64_i32 v[32:33], s[10:11], v40, s3, v[216:217]
	v_mad_i64_i32 v[34:35], s[10:11], v41, s3, v[216:217]
	v_mad_i64_i32 v[44:45], s[10:11], v42, s3, v[216:217]
	v_mad_i64_i32 v[46:47], s[10:11], v43, s3, v[216:217]
	global_load_dwordx4 v[112:115], v[32:33], off offset:-4096
	global_load_dwordx4 v[116:119], v[32:33], off
	global_load_dwordx4 v[120:123], v[34:35], off offset:-4096
	global_load_dwordx4 v[124:127], v[34:35], off
	global_load_dwordx4 v[128:131], v[44:45], off offset:-4096
	global_load_dwordx4 v[132:135], v[44:45], off
	global_load_dwordx4 v[136:139], v[46:47], off offset:-4096
	global_load_dwordx4 v[140:143], v[46:47], off
	v_mov_b32_e32 v48, 0
	s_mov_b32 s58, 0
	v_mov_b32_e32 v205, 1.0
	v_mov_b32_e32 v49, v48
	v_mov_b32_e32 v50, v48
	v_mov_b32_e32 v51, v48
	v_mov_b32_e32 v52, v48
	v_mov_b32_e32 v53, v48
	v_mov_b32_e32 v54, v48
	v_mov_b32_e32 v55, v48
	v_mov_b32_e32 v56, v48
	v_mov_b32_e32 v57, v48
	v_mov_b32_e32 v58, v48
	v_mov_b32_e32 v59, v48
	v_mov_b32_e32 v60, v48
	v_mov_b32_e32 v61, v48
	v_mov_b32_e32 v62, v48
	s_add_i32 s10, s43, s14
	s_and_b32 s10, s10, 0xfffff000
	s_or_b32 s10, s56, s10
	s_waitcnt vmcnt(16)
	ds_write_b128 v190, v[0:3] offset:8192
	ds_write_b128 v191, v[4:7] offset:8192
	ds_write_b128 v192, v[8:11] offset:8192
	ds_write_b128 v193, v[12:15] offset:8192
	ds_write_b128 v194, v[16:19] offset:8192
	ds_write_b128 v195, v[20:23] offset:8192
	ds_write_b128 v196, v[24:27] offset:8192
	ds_write_b128 v197, v[28:31] offset:8192
	v_add_u32_e32 v147, s10, v182
	v_add_u32_e32 v198, s10, v183
	v_add_u32_e32 v199, s10, v184
	v_add_u32_e32 v200, s10, v185
	v_add_u32_e32 v201, s10, v186
	v_add_u32_e32 v202, s10, v187
	v_add_u32_e32 v203, s10, v188
	v_add_u32_e32 v204, s10, v189
	v_mov_b32_e32 v63, v48
	v_mov_b32_e32 v32, v48
	v_mov_b32_e32 v33, v48
	v_mov_b32_e32 v34, v48
	v_mov_b32_e32 v35, v48
	v_mov_b32_e32 v36, v48
	v_mov_b32_e32 v37, v48
	v_mov_b32_e32 v38, v48
	v_mov_b32_e32 v39, v48
	v_mov_b32_e32 v40, v48
	v_mov_b32_e32 v41, v48
	v_mov_b32_e32 v42, v48
	v_mov_b32_e32 v43, v48
	v_mov_b32_e32 v44, v48
	v_mov_b32_e32 v45, v48
	v_mov_b32_e32 v46, v48
	v_mov_b32_e32 v47, v48
	v_mov_b32_e32 v16, v48
	v_mov_b32_e32 v17, v48
	v_mov_b32_e32 v18, v48
	v_mov_b32_e32 v19, v48
	v_mov_b32_e32 v20, v48
	v_mov_b32_e32 v21, v48
	v_mov_b32_e32 v22, v48
	v_mov_b32_e32 v23, v48
	v_mov_b32_e32 v24, v48
	v_mov_b32_e32 v25, v48
	v_mov_b32_e32 v26, v48
	v_mov_b32_e32 v27, v48
	v_mov_b32_e32 v28, v48
	v_mov_b32_e32 v29, v48
	v_mov_b32_e32 v30, v48
	v_mov_b32_e32 v31, v48
	v_mov_b32_e32 v0, v48
	v_mov_b32_e32 v1, v48
	v_mov_b32_e32 v2, v48
	v_mov_b32_e32 v3, v48
	v_mov_b32_e32 v4, v48
	v_mov_b32_e32 v5, v48
	v_mov_b32_e32 v6, v48
	v_mov_b32_e32 v7, v48
	v_mov_b32_e32 v8, v48
	v_mov_b32_e32 v9, v48
	v_mov_b32_e32 v10, v48
	v_mov_b32_e32 v11, v48
	v_mov_b32_e32 v12, v48
	v_mov_b32_e32 v13, v48
	v_mov_b32_e32 v14, v48
	v_mov_b32_e32 v15, v48
	s_branch .LBB0_455
